# phase 5 GEMM epilogue: all 16 gate-row loads issued at the start of the epilogue into unused VGPRs (no load queues behind a store in the in-order vmcnt queue); on top of hoisted GEMM constants, unscal
# speedup vs baseline: 1.0024x; 1.0024x over previous
.LBB0_2179:
	s_lshl_b32 s6, s56, 8
	v_mbcnt_lo_u32_b32 v128, -1, 0
	v_mbcnt_hi_u32_b32 v128, -1, v128
	s_add_i32 s6, s6, s45
	v_and_or_b32 v130, v128, 15, s6
	s_lshl_b32 s6, s55, 8
	v_ashrrev_i32_e32 v128, 1, v128
	s_or_b32 s6, s6, s46
	v_and_b32_e32 v128, -8, v128
	v_add_u32_e32 v128, s6, v128
	v_mov_b64_e32 v[132:133], s[12:13]
	v_ashrrev_i32_e32 v129, 31, v128
	v_mad_i64_i32 v[136:137], s[6:7], v130, s51, v[132:133]
	v_lshlrev_b64 v[128:129], 1, v[128:129]
	v_lshl_add_u64 v[140:141], v[136:137], 0, v[128:129]
	s_mov_b32 s100, 0x6a000
	s_mov_b32 s101, 0
	global_load_dwordx4 v[176:179], v[140:141], off
	global_load_dwordx4 v[180:183], v[140:141], off offset:256
	v_lshl_add_u64 v[240:241], v[140:141], 0, s[100:101]
	global_load_dwordx4 v[184:187], v[240:241], off
	global_load_dwordx4 v[188:191], v[240:241], off offset:256
	v_lshl_add_u64 v[240:241], v[240:241], 0, s[100:101]
	global_load_dwordx4 v[192:195], v[240:241], off
	global_load_dwordx4 v[196:199], v[240:241], off offset:256
	v_lshl_add_u64 v[240:241], v[240:241], 0, s[100:101]
	global_load_dwordx4 v[200:203], v[240:241], off
	global_load_dwordx4 v[204:207], v[240:241], off offset:256
	s_mov_b32 s100, 0x212000
	v_lshl_add_u64 v[240:241], v[240:241], 0, s[100:101]
	global_load_dwordx4 v[208:211], v[240:241], off
	global_load_dwordx4 v[212:215], v[240:241], off offset:256
	s_mov_b32 s100, 0x6a000
	v_lshl_add_u64 v[240:241], v[240:241], 0, s[100:101]
	global_load_dwordx4 v[216:219], v[240:241], off
	global_load_dwordx4 v[220:223], v[240:241], off offset:256
	v_lshl_add_u64 v[240:241], v[240:241], 0, s[100:101]
	global_load_dwordx4 v[224:227], v[240:241], off
	global_load_dwordx4 v[228:231], v[240:241], off offset:256
	v_lshl_add_u64 v[240:241], v[240:241], 0, s[100:101]
	global_load_dwordx4 v[232:235], v[240:241], off
	global_load_dwordx4 v[236:239], v[240:241], off offset:256
	s_nop 0
	v_or_b32_e32 v156, 16, v130
	v_pk_mul_f32 v[154:155], v[112:113], s[16:17] op_sel_hi:[1,0]
	v_mad_i64_i32 v[112:113], s[6:7], v156, s51, v[132:133]
	v_lshl_add_u64 v[112:113], v[112:113], 0, v[128:129]
	v_pk_mul_f32 v[144:145], v[122:123], s[16:17] op_sel_hi:[1,0]
	v_pk_mul_f32 v[146:147], v[120:121], s[16:17] op_sel_hi:[1,0]
	v_pk_mul_f32 v[148:149], v[118:119], s[16:17] op_sel_hi:[1,0]
	v_pk_mul_f32 v[150:151], v[116:117], s[16:17] op_sel_hi:[1,0]
	v_ashrrev_i32_e32 v131, 31, v130
	v_pk_mul_f32 v[152:153], v[114:115], s[16:17] op_sel_hi:[1,0]
	v_lshlrev_b64 v[114:115], 12, v[130:131]
	v_lshl_add_u64 v[114:115], s[2:3], 0, v[114:115]
	v_lshl_add_u64 v[158:159], v[114:115], 0, v[128:129]
	v_pk_mul_f32 v[126:127], v[126:127], s[16:17] op_sel_hi:[1,0]
	v_pk_mul_f32 v[124:125], v[124:125], s[16:17] op_sel_hi:[1,0]
	v_pk_mul_f32 v[108:109], v[108:109], s[16:17] op_sel_hi:[1,0]
	v_pk_mul_f32 v[110:111], v[110:111], s[16:17] op_sel_hi:[1,0]
	v_ashrrev_i32_e32 v157, 31, v156
	v_pk_mul_f32 v[106:107], v[106:107], s[16:17] op_sel_hi:[1,0]
	v_pk_mul_f32 v[104:105], v[104:105], s[16:17] op_sel_hi:[1,0]
	v_pk_mul_f32 v[102:103], v[102:103], s[16:17] op_sel_hi:[1,0]
	v_pk_mul_f32 v[100:101], v[100:101], s[16:17] op_sel_hi:[1,0]
	v_pk_mul_f32 v[96:97], v[96:97], s[16:17] op_sel_hi:[1,0]
	v_pk_mul_f32 v[98:99], v[98:99], s[16:17] op_sel_hi:[1,0]
	v_pk_mul_f32 v[94:95], v[94:95], s[16:17] op_sel_hi:[1,0]
	v_pk_mul_f32 v[92:93], v[92:93], s[16:17] op_sel_hi:[1,0]
	v_pk_mul_f32 v[90:91], v[90:91], s[16:17] op_sel_hi:[1,0]
	v_pk_mul_f32 v[88:89], v[88:89], s[16:17] op_sel_hi:[1,0]
	v_pk_mul_f32 v[86:87], v[86:87], s[16:17] op_sel_hi:[1,0]
	v_pk_mul_f32 v[84:85], v[84:85], s[16:17] op_sel_hi:[1,0]
	v_pk_mul_f32 v[80:81], v[80:81], s[16:17] op_sel_hi:[1,0]
	v_pk_mul_f32 v[82:83], v[82:83], s[16:17] op_sel_hi:[1,0]
	v_pk_mul_f32 v[78:79], v[78:79], s[16:17] op_sel_hi:[1,0]
	v_pk_mul_f32 v[76:77], v[76:77], s[16:17] op_sel_hi:[1,0]
	v_pk_mul_f32 v[74:75], v[74:75], s[16:17] op_sel_hi:[1,0]
	v_pk_mul_f32 v[72:73], v[72:73], s[16:17] op_sel_hi:[1,0]
	v_pk_mul_f32 v[70:71], v[70:71], s[16:17] op_sel_hi:[1,0]
	v_pk_mul_f32 v[68:69], v[68:69], s[16:17] op_sel_hi:[1,0]
	v_pk_mul_f32 v[64:65], v[64:65], s[16:17] op_sel_hi:[1,0]
	v_pk_mul_f32 v[66:67], v[66:67], s[16:17] op_sel_hi:[1,0]
	v_pk_mul_f32 v[62:63], v[62:63], s[16:17] op_sel_hi:[1,0]
	v_pk_mul_f32 v[60:61], v[60:61], s[16:17] op_sel_hi:[1,0]
	v_pk_mul_f32 v[58:59], v[58:59], s[16:17] op_sel_hi:[1,0]
	v_pk_mul_f32 v[56:57], v[56:57], s[16:17] op_sel_hi:[1,0]
	v_pk_mul_f32 v[54:55], v[54:55], s[16:17] op_sel_hi:[1,0]
	v_pk_mul_f32 v[52:53], v[52:53], s[16:17] op_sel_hi:[1,0]
	v_pk_mul_f32 v[48:49], v[48:49], s[16:17] op_sel_hi:[1,0]
	v_pk_mul_f32 v[50:51], v[50:51], s[16:17] op_sel_hi:[1,0]
	v_pk_mul_f32 v[46:47], v[46:47], s[16:17] op_sel_hi:[1,0]
	v_pk_mul_f32 v[44:45], v[44:45], s[16:17] op_sel_hi:[1,0]
	v_pk_mul_f32 v[42:43], v[42:43], s[16:17] op_sel_hi:[1,0]
	v_pk_mul_f32 v[40:41], v[40:41], s[16:17] op_sel_hi:[1,0]
	v_pk_mul_f32 v[38:39], v[38:39], s[16:17] op_sel_hi:[1,0]
	v_pk_mul_f32 v[36:37], v[36:37], s[16:17] op_sel_hi:[1,0]
	v_pk_mul_f32 v[32:33], v[32:33], s[16:17] op_sel_hi:[1,0]
	v_pk_mul_f32 v[34:35], v[34:35], s[16:17] op_sel_hi:[1,0]
	v_pk_mul_f32 v[30:31], v[30:31], s[16:17] op_sel_hi:[1,0]
	v_pk_mul_f32 v[28:29], v[28:29], s[16:17] op_sel_hi:[1,0]
	v_pk_mul_f32 v[26:27], v[26:27], s[16:17] op_sel_hi:[1,0]
	v_pk_mul_f32 v[24:25], v[24:25], s[16:17] op_sel_hi:[1,0]
	v_pk_mul_f32 v[22:23], v[22:23], s[16:17] op_sel_hi:[1,0]
	v_pk_mul_f32 v[20:21], v[20:21], s[16:17] op_sel_hi:[1,0]
	v_pk_mul_f32 v[18:19], v[18:19], s[16:17] op_sel_hi:[1,0]
	v_pk_mul_f32 v[16:17], v[16:17], s[16:17] op_sel_hi:[1,0]
	v_pk_mul_f32 v[14:15], v[14:15], s[16:17] op_sel_hi:[1,0]
	v_pk_mul_f32 v[12:13], v[12:13], s[16:17] op_sel_hi:[1,0]
	v_pk_mul_f32 v[10:11], v[10:11], s[16:17] op_sel_hi:[1,0]
	v_pk_mul_f32 v[8:9], v[8:9], s[16:17] op_sel_hi:[1,0]
	v_pk_mul_f32 v[6:7], v[6:7], s[16:17] op_sel_hi:[1,0]
	v_pk_mul_f32 v[4:5], v[4:5], s[16:17] op_sel_hi:[1,0]
	v_pk_mul_f32 v[2:3], v[2:3], s[16:17] op_sel_hi:[1,0]
	v_pk_mul_f32 v[0:1], v[0:1], s[16:17] op_sel_hi:[1,0]
	s_andn2_b64 vcc, exec, s[18:19]
	s_waitcnt vmcnt(15)
	v_lshlrev_b32_e32 v112, 16, v176
	v_and_b32_e32 v113, 0xffff0000, v176
	v_lshlrev_b32_e32 v114, 16, v177
	v_and_b32_e32 v115, 0xffff0000, v177
	v_lshlrev_b32_e32 v131, 16, v178
	v_and_b32_e32 v136, 0xffff0000, v178
	v_mul_f32_e32 v112, 0xbfb8aa3b, v112
	v_mul_f32_e32 v113, 0xbfb8aa3b, v113
	v_mul_f32_e32 v114, 0xbfb8aa3b, v114
	v_lshlrev_b32_e32 v137, 16, v179
	v_and_b32_e32 v138, 0xffff0000, v179
	v_mul_f32_e32 v115, 0xbfb8aa3b, v115
	v_mul_f32_e32 v131, 0xbfb8aa3b, v131
	v_mul_f32_e32 v136, 0xbfb8aa3b, v136
	v_exp_f32_e32 v112, v112
	v_exp_f32_e32 v113, v113
	v_exp_f32_e32 v114, v114
	v_mul_f32_e32 v137, 0xbfb8aa3b, v137
	v_mul_f32_e32 v138, 0xbfb8aa3b, v138
	v_exp_f32_e32 v115, v115
	v_exp_f32_e32 v131, v131
	v_exp_f32_e32 v136, v136
	v_exp_f32_e32 v137, v137
	v_exp_f32_e32 v138, v138
	v_add_f32_e32 v112, 1.0, v112
	v_add_f32_e32 v113, 1.0, v113
	v_add_f32_e32 v114, 1.0, v114
	v_add_f32_e32 v115, 1.0, v115
	v_add_f32_e32 v131, 1.0, v131
	v_add_f32_e32 v136, 1.0, v136
	v_rcp_f32_e32 v112, v112
	v_rcp_f32_e32 v113, v113
	v_rcp_f32_e32 v114, v114
	v_add_f32_e32 v137, 1.0, v137
	v_add_f32_e32 v138, 1.0, v138
	v_rcp_f32_e32 v115, v115
	v_rcp_f32_e32 v131, v131
	v_rcp_f32_e32 v136, v136
	v_rcp_f32_e32 v137, v137
	v_rcp_f32_e32 v138, v138
	v_mul_f32_e32 v112, v124, v112
	v_mul_f32_e32 v113, v125, v113
	v_mul_f32_e32 v114, v126, v114
	s_waitcnt vmcnt(14)
	v_lshlrev_b32_e32 v139, 16, v180
	v_and_b32_e32 v140, 0xffff0000, v180
	v_lshlrev_b32_e32 v160, 16, v181
	v_mul_f32_e32 v115, v127, v115
	v_mul_f32_e32 v124, v146, v131
	v_mul_f32_e32 v125, v147, v136
	v_cvt_pk_bf16_f32 v112, v112, v113
	v_cvt_pk_bf16_f32 v113, v114, v115
	v_cvt_pk_bf16_f32 v114, v124, v125
	v_mul_f32_e32 v140, 0xbfb8aa3b, v140
	v_mul_f32_e32 v160, 0xbfb8aa3b, v160
	v_mul_f32_e32 v126, v144, v137
	v_mul_f32_e32 v127, v145, v138
	v_cvt_pk_bf16_f32 v115, v126, v127
	global_store_dwordx4 v[158:159], v[112:115], off
	v_mul_f32_e32 v139, 0xbfb8aa3b, v139
	v_exp_f32_e32 v140, v140
	v_and_b32_e32 v114, 0xffff0000, v181
	v_exp_f32_e32 v160, v160
	v_mul_f32_e32 v114, 0xbfb8aa3b, v114
	v_lshlrev_b32_e32 v124, 16, v182
	v_and_b32_e32 v125, 0xffff0000, v182
	v_lshlrev_b32_e32 v126, 16, v183
	v_and_b32_e32 v127, 0xffff0000, v183
	v_exp_f32_e32 v139, v139
	v_exp_f32_e32 v114, v114
	v_mul_f32_e32 v124, 0xbfb8aa3b, v124
	v_mul_f32_e32 v125, 0xbfb8aa3b, v125
	v_mul_f32_e32 v126, 0xbfb8aa3b, v126
	v_mul_f32_e32 v127, 0xbfb8aa3b, v127
	v_exp_f32_e32 v124, v124
	v_exp_f32_e32 v125, v125
	v_exp_f32_e32 v126, v126
	v_exp_f32_e32 v127, v127
	v_add_f32_e32 v140, 1.0, v140
	v_add_f32_e32 v113, 1.0, v160
	v_add_f32_e32 v139, 1.0, v139
	v_rcp_f32_e32 v112, v140
	v_rcp_f32_e32 v113, v113
	v_add_f32_e32 v114, 1.0, v114
	v_rcp_f32_e32 v139, v139
	v_rcp_f32_e32 v114, v114
	v_add_f32_e32 v124, 1.0, v124
	v_add_f32_e32 v125, 1.0, v125
	v_add_f32_e32 v126, 1.0, v126
	v_add_f32_e32 v127, 1.0, v127
	v_rcp_f32_e32 v124, v124
	v_rcp_f32_e32 v125, v125
	v_rcp_f32_e32 v126, v126
	v_rcp_f32_e32 v127, v127
	v_mul_f32_e32 v112, v151, v112
	v_mul_f32_e32 v113, v148, v113
	v_mul_f32_e32 v115, v150, v139
	v_mul_f32_e32 v114, v149, v114
	v_cvt_pk_bf16_f32 v112, v115, v112
	v_cvt_pk_bf16_f32 v113, v113, v114
	v_or_b32_e32 v136, 32, v130
	v_mul_f32_e32 v124, v154, v124
	v_mul_f32_e32 v125, v155, v125
	v_mul_f32_e32 v126, v152, v126
	v_mul_f32_e32 v127, v153, v127
	v_cvt_pk_bf16_f32 v114, v124, v125
	v_cvt_pk_bf16_f32 v115, v126, v127
	global_store_dwordx4 v[158:159], v[112:115], off offset:256
	s_waitcnt vmcnt(15)
	v_lshlrev_b32_e32 v131, 16, v184
	v_and_b32_e32 v120, 0xffff0000, v184
	v_mad_i64_i32 v[112:113], s[6:7], v136, s51, v[132:133]
	v_lshl_add_u64 v[112:113], v[112:113], 0, v[128:129]
	v_mul_f32_e32 v120, 0xbfb8aa3b, v120
	s_nop 0
	v_exp_f32_e32 v120, v120
	v_lshlrev_b32_e32 v140, 16, v185
	v_and_b32_e32 v121, 0xffff0000, v185
	v_mul_f32_e32 v121, 0xbfb8aa3b, v121
	v_add_f32_e32 v120, 1.0, v120
	v_rcp_f32_e32 v120, v120
	v_exp_f32_e32 v121, v121
	v_mul_f32_e32 v131, 0xbfb8aa3b, v131
	v_mul_f32_e32 v140, 0xbfb8aa3b, v140
	v_mul_f32_e32 v109, v109, v120
	v_add_f32_e32 v120, 1.0, v121
	v_lshlrev_b32_e32 v121, 16, v186
	v_and_b32_e32 v122, 0xffff0000, v186
	v_mul_f32_e32 v121, 0xbfb8aa3b, v121
	v_mul_f32_e32 v122, 0xbfb8aa3b, v122
	v_rcp_f32_e32 v120, v120
	v_exp_f32_e32 v121, v121
	v_exp_f32_e32 v122, v122
	v_exp_f32_e32 v131, v131
	v_mul_f32_e32 v111, v111, v120
	v_add_f32_e32 v120, 1.0, v121
	v_add_f32_e32 v121, 1.0, v122
	v_lshlrev_b32_e32 v122, 16, v187
	v_and_b32_e32 v123, 0xffff0000, v187
	v_mul_f32_e32 v122, 0xbfb8aa3b, v122
	v_mul_f32_e32 v123, 0xbfb8aa3b, v123
	v_exp_f32_e32 v140, v140
	v_exp_f32_e32 v122, v122
	v_exp_f32_e32 v123, v123
	v_add_f32_e32 v131, 1.0, v131
	v_add_f32_e32 v140, 1.0, v140
	v_add_f32_e32 v122, 1.0, v122
	v_add_f32_e32 v123, 1.0, v123
	v_rcp_f32_e32 v131, v131
	v_rcp_f32_e32 v140, v140
	v_rcp_f32_e32 v120, v120
	v_rcp_f32_e32 v121, v121
	v_rcp_f32_e32 v122, v122
	v_rcp_f32_e32 v123, v123
	v_lshlrev_b64 v[138:139], 12, v[156:157]
	v_lshl_add_u64 v[138:139], s[2:3], 0, v[138:139]
	v_lshl_add_u64 v[138:139], v[138:139], 0, v[128:129]
	v_mul_f32_e32 v108, v108, v131
	v_mul_f32_e32 v110, v110, v140
	v_mul_f32_e32 v120, v104, v120
	v_mul_f32_e32 v121, v105, v121
	v_mul_f32_e32 v122, v106, v122
	v_mul_f32_e32 v107, v107, v123
	v_cvt_pk_bf16_f32 v104, v108, v109
	v_cvt_pk_bf16_f32 v105, v110, v111
	v_cvt_pk_bf16_f32 v106, v120, v121
	v_cvt_pk_bf16_f32 v107, v122, v107
	global_store_dwordx4 v[138:139], v[104:107], off
	v_ashrrev_i32_e32 v137, 31, v136
	s_waitcnt vmcnt(14)
	v_and_b32_e32 v109, 0xffff0000, v192
	v_and_b32_e32 v105, 0xffff0000, v188
	v_lshlrev_b32_e32 v106, 16, v189
	v_lshlrev_b32_e32 v104, 16, v188
	v_mul_f32_e32 v105, 0xbfb8aa3b, v105
	v_mul_f32_e32 v106, 0xbfb8aa3b, v106
	v_mul_f32_e32 v104, 0xbfb8aa3b, v104
	v_exp_f32_e32 v105, v105
	v_exp_f32_e32 v106, v106
	v_exp_f32_e32 v104, v104
	v_and_b32_e32 v107, 0xffff0000, v189
	v_add_f32_e32 v105, 1.0, v105
	v_add_f32_e32 v106, 1.0, v106
	v_add_f32_e32 v104, 1.0, v104
	v_rcp_f32_e32 v105, v105
	v_rcp_f32_e32 v106, v106
	v_mul_f32_e32 v107, 0xbfb8aa3b, v107
	v_rcp_f32_e32 v104, v104
	v_exp_f32_e32 v107, v107
	v_mul_f32_e32 v101, v101, v105
	v_mul_f32_e32 v102, v102, v106
	v_lshlrev_b32_e32 v105, 16, v190
	v_and_b32_e32 v106, 0xffff0000, v190
	v_mul_f32_e32 v100, v100, v104
	v_add_f32_e32 v104, 1.0, v107
	v_mul_f32_e32 v105, 0xbfb8aa3b, v105
	v_mul_f32_e32 v106, 0xbfb8aa3b, v106
	v_rcp_f32_e32 v104, v104
	v_exp_f32_e32 v105, v105
	v_exp_f32_e32 v106, v106
	v_and_b32_e32 v107, 0xffff0000, v191
	v_mul_f32_e32 v103, v103, v104
	v_add_f32_e32 v104, 1.0, v105
	v_add_f32_e32 v105, 1.0, v106
	v_lshlrev_b32_e32 v106, 16, v191
	v_mul_f32_e32 v106, 0xbfb8aa3b, v106
	v_mul_f32_e32 v107, 0xbfb8aa3b, v107
	v_exp_f32_e32 v106, v106
	v_exp_f32_e32 v107, v107
	v_rcp_f32_e32 v104, v104
	v_rcp_f32_e32 v105, v105
	v_add_f32_e32 v106, 1.0, v106
	v_add_f32_e32 v107, 1.0, v107
	v_rcp_f32_e32 v106, v106
	v_rcp_f32_e32 v107, v107
	v_mul_f32_e32 v104, v96, v104
	v_mul_f32_e32 v105, v97, v105
	v_mul_f32_e32 v106, v98, v106
	v_mul_f32_e32 v99, v99, v107
	v_cvt_pk_bf16_f32 v96, v100, v101
	v_cvt_pk_bf16_f32 v97, v102, v103
	v_cvt_pk_bf16_f32 v98, v104, v105
	v_or_b32_e32 v104, 48, v130
	v_cvt_pk_bf16_f32 v99, v106, v99
	global_store_dwordx4 v[138:139], v[96:99], off offset:256
	v_lshlrev_b32_e32 v110, 16, v193
	v_lshlrev_b32_e32 v108, 16, v192
	v_mad_i64_i32 v[96:97], s[6:7], v104, s51, v[132:133]
	v_lshl_add_u64 v[96:97], v[96:97], 0, v[128:129]
	s_nop 0
	v_mul_f32_e32 v109, 0xbfb8aa3b, v109
	v_mul_f32_e32 v110, 0xbfb8aa3b, v110
	v_mul_f32_e32 v108, 0xbfb8aa3b, v108
	v_exp_f32_e32 v109, v109
	v_exp_f32_e32 v110, v110
	v_exp_f32_e32 v108, v108
	v_and_b32_e32 v111, 0xffff0000, v193
	v_add_f32_e32 v109, 1.0, v109
	v_add_f32_e32 v110, 1.0, v110
	v_add_f32_e32 v108, 1.0, v108
	v_rcp_f32_e32 v109, v109
	v_rcp_f32_e32 v110, v110
	v_mul_f32_e32 v111, 0xbfb8aa3b, v111
	v_rcp_f32_e32 v108, v108
	v_exp_f32_e32 v111, v111
	v_mul_f32_e32 v93, v93, v109
	v_mul_f32_e32 v94, v94, v110
	v_lshlrev_b32_e32 v109, 16, v194
	v_and_b32_e32 v110, 0xffff0000, v194
	v_mul_f32_e32 v92, v92, v108
	v_add_f32_e32 v108, 1.0, v111
	v_mul_f32_e32 v109, 0xbfb8aa3b, v109
	v_mul_f32_e32 v110, 0xbfb8aa3b, v110
	v_rcp_f32_e32 v108, v108
	v_exp_f32_e32 v109, v109
	v_exp_f32_e32 v110, v110
	v_and_b32_e32 v111, 0xffff0000, v195
	v_mul_f32_e32 v95, v95, v108
	v_add_f32_e32 v108, 1.0, v109
	v_add_f32_e32 v109, 1.0, v110
	v_lshlrev_b32_e32 v110, 16, v195
	v_mul_f32_e32 v110, 0xbfb8aa3b, v110
	v_mul_f32_e32 v111, 0xbfb8aa3b, v111
	v_exp_f32_e32 v110, v110
	v_exp_f32_e32 v111, v111
	v_rcp_f32_e32 v108, v108
	v_rcp_f32_e32 v109, v109
	v_add_f32_e32 v110, 1.0, v110
	v_add_f32_e32 v111, 1.0, v111
	v_rcp_f32_e32 v110, v110
	v_rcp_f32_e32 v111, v111
	v_lshlrev_b64 v[106:107], 12, v[136:137]
	v_lshl_add_u64 v[106:107], s[2:3], 0, v[106:107]
	v_lshl_add_u64 v[106:107], v[106:107], 0, v[128:129]
	v_mul_f32_e32 v108, v88, v108
	v_mul_f32_e32 v109, v89, v109
	v_mul_f32_e32 v110, v90, v110
	v_mul_f32_e32 v91, v91, v111
	v_cvt_pk_bf16_f32 v88, v92, v93
	v_cvt_pk_bf16_f32 v89, v94, v95
	v_cvt_pk_bf16_f32 v90, v108, v109
	v_cvt_pk_bf16_f32 v91, v110, v91
	global_store_dwordx4 v[106:107], v[88:91], off
	v_ashrrev_i32_e32 v105, 31, v104
	s_waitcnt vmcnt(14)
	v_and_b32_e32 v93, 0xffff0000, v200
	v_and_b32_e32 v89, 0xffff0000, v196
	v_lshlrev_b32_e32 v90, 16, v197
	v_lshlrev_b32_e32 v88, 16, v196
	v_mul_f32_e32 v89, 0xbfb8aa3b, v89
	v_mul_f32_e32 v90, 0xbfb8aa3b, v90
	v_mul_f32_e32 v88, 0xbfb8aa3b, v88
	v_exp_f32_e32 v89, v89
	v_exp_f32_e32 v90, v90
	v_exp_f32_e32 v88, v88
	v_and_b32_e32 v91, 0xffff0000, v197
	v_add_f32_e32 v89, 1.0, v89
	v_add_f32_e32 v90, 1.0, v90
	v_add_f32_e32 v88, 1.0, v88
	v_rcp_f32_e32 v89, v89
	v_rcp_f32_e32 v90, v90
	v_mul_f32_e32 v91, 0xbfb8aa3b, v91
	v_rcp_f32_e32 v88, v88
	v_exp_f32_e32 v91, v91
	v_mul_f32_e32 v85, v85, v89
	v_mul_f32_e32 v86, v86, v90
	v_lshlrev_b32_e32 v89, 16, v198
	v_and_b32_e32 v90, 0xffff0000, v198
	v_mul_f32_e32 v84, v84, v88
	v_add_f32_e32 v88, 1.0, v91
	v_mul_f32_e32 v89, 0xbfb8aa3b, v89
	v_mul_f32_e32 v90, 0xbfb8aa3b, v90
	v_rcp_f32_e32 v88, v88
	v_exp_f32_e32 v89, v89
	v_exp_f32_e32 v90, v90
	v_and_b32_e32 v91, 0xffff0000, v199
	v_mul_f32_e32 v87, v87, v88
	v_add_f32_e32 v88, 1.0, v89
	v_add_f32_e32 v89, 1.0, v90
	v_lshlrev_b32_e32 v90, 16, v199
	v_mul_f32_e32 v90, 0xbfb8aa3b, v90
	v_mul_f32_e32 v91, 0xbfb8aa3b, v91
	v_exp_f32_e32 v90, v90
	v_exp_f32_e32 v91, v91
	v_rcp_f32_e32 v88, v88
	v_rcp_f32_e32 v89, v89
	v_add_f32_e32 v90, 1.0, v90
	v_add_f32_e32 v91, 1.0, v91
	v_rcp_f32_e32 v90, v90
	v_rcp_f32_e32 v91, v91
	v_mul_f32_e32 v88, v80, v88
	v_mul_f32_e32 v89, v81, v89
	v_mul_f32_e32 v90, v82, v90
	v_mul_f32_e32 v83, v83, v91
	v_cvt_pk_bf16_f32 v80, v84, v85
	v_cvt_pk_bf16_f32 v81, v86, v87
	v_cvt_pk_bf16_f32 v82, v88, v89
	v_add_u32_e32 v88, 0x80, v130
	v_cvt_pk_bf16_f32 v83, v90, v83
	global_store_dwordx4 v[106:107], v[80:83], off offset:256
	v_lshlrev_b32_e32 v94, 16, v201
	v_lshlrev_b32_e32 v92, 16, v200
	v_mad_i64_i32 v[80:81], s[6:7], v88, s51, v[132:133]
	v_lshl_add_u64 v[80:81], v[80:81], 0, v[128:129]
	v_mul_f32_e32 v93, 0xbfb8aa3b, v93
	v_mul_f32_e32 v94, 0xbfb8aa3b, v94
	s_nop 0
	v_mul_f32_e32 v92, 0xbfb8aa3b, v92
	v_exp_f32_e32 v93, v93
	v_exp_f32_e32 v94, v94
	v_exp_f32_e32 v92, v92
	v_and_b32_e32 v95, 0xffff0000, v201
	v_add_f32_e32 v93, 1.0, v93
	v_add_f32_e32 v94, 1.0, v94
	v_add_f32_e32 v92, 1.0, v92
	v_rcp_f32_e32 v93, v93
	v_rcp_f32_e32 v94, v94
	v_mul_f32_e32 v95, 0xbfb8aa3b, v95
	v_rcp_f32_e32 v92, v92
	v_exp_f32_e32 v95, v95
	v_mul_f32_e32 v77, v77, v93
	v_mul_f32_e32 v78, v78, v94
	v_lshlrev_b32_e32 v93, 16, v202
	v_and_b32_e32 v94, 0xffff0000, v202
	v_mul_f32_e32 v76, v76, v92
	v_add_f32_e32 v92, 1.0, v95
	v_mul_f32_e32 v93, 0xbfb8aa3b, v93
	v_mul_f32_e32 v94, 0xbfb8aa3b, v94
	v_rcp_f32_e32 v92, v92
	v_exp_f32_e32 v93, v93
	v_exp_f32_e32 v94, v94
	v_and_b32_e32 v95, 0xffff0000, v203
	v_mul_f32_e32 v79, v79, v92
	v_add_f32_e32 v92, 1.0, v93
	v_add_f32_e32 v93, 1.0, v94
	v_lshlrev_b32_e32 v94, 16, v203
	v_mul_f32_e32 v94, 0xbfb8aa3b, v94
	v_mul_f32_e32 v95, 0xbfb8aa3b, v95
	v_exp_f32_e32 v94, v94
	v_exp_f32_e32 v95, v95
	v_rcp_f32_e32 v92, v92
	v_rcp_f32_e32 v93, v93
	v_add_f32_e32 v94, 1.0, v94
	v_add_f32_e32 v95, 1.0, v95
	v_rcp_f32_e32 v94, v94
	v_rcp_f32_e32 v95, v95
	v_lshlrev_b64 v[90:91], 12, v[104:105]
	v_lshl_add_u64 v[90:91], s[2:3], 0, v[90:91]
	v_lshl_add_u64 v[90:91], v[90:91], 0, v[128:129]
	v_mul_f32_e32 v92, v72, v92
	v_mul_f32_e32 v93, v73, v93
	v_mul_f32_e32 v94, v74, v94
	v_mul_f32_e32 v75, v75, v95
	v_cvt_pk_bf16_f32 v72, v76, v77
	v_cvt_pk_bf16_f32 v73, v78, v79
	v_cvt_pk_bf16_f32 v74, v92, v93
	v_cvt_pk_bf16_f32 v75, v94, v75
	global_store_dwordx4 v[90:91], v[72:75], off
	v_ashrrev_i32_e32 v89, 31, v88
	s_waitcnt vmcnt(14)
	v_and_b32_e32 v77, 0xffff0000, v208
	v_and_b32_e32 v73, 0xffff0000, v204
	v_lshlrev_b32_e32 v74, 16, v205
	v_lshlrev_b32_e32 v72, 16, v204
	v_mul_f32_e32 v73, 0xbfb8aa3b, v73
	v_mul_f32_e32 v74, 0xbfb8aa3b, v74
	v_mul_f32_e32 v72, 0xbfb8aa3b, v72
	v_exp_f32_e32 v73, v73
	v_exp_f32_e32 v74, v74
	v_exp_f32_e32 v72, v72
	v_and_b32_e32 v75, 0xffff0000, v205
	v_add_f32_e32 v73, 1.0, v73
	v_add_f32_e32 v74, 1.0, v74
	v_add_f32_e32 v72, 1.0, v72
	v_rcp_f32_e32 v73, v73
	v_rcp_f32_e32 v74, v74
	v_mul_f32_e32 v75, 0xbfb8aa3b, v75
	v_rcp_f32_e32 v72, v72
	v_exp_f32_e32 v75, v75
	v_mul_f32_e32 v69, v69, v73
	v_mul_f32_e32 v70, v70, v74
	v_lshlrev_b32_e32 v73, 16, v206
	v_and_b32_e32 v74, 0xffff0000, v206
	v_mul_f32_e32 v68, v68, v72
	v_add_f32_e32 v72, 1.0, v75
	v_mul_f32_e32 v73, 0xbfb8aa3b, v73
	v_mul_f32_e32 v74, 0xbfb8aa3b, v74
	v_rcp_f32_e32 v72, v72
	v_exp_f32_e32 v73, v73
	v_exp_f32_e32 v74, v74
	v_and_b32_e32 v75, 0xffff0000, v207
	v_mul_f32_e32 v71, v71, v72
	v_add_f32_e32 v72, 1.0, v73
	v_add_f32_e32 v73, 1.0, v74
	v_lshlrev_b32_e32 v74, 16, v207
	v_mul_f32_e32 v74, 0xbfb8aa3b, v74
	v_mul_f32_e32 v75, 0xbfb8aa3b, v75
	v_exp_f32_e32 v74, v74
	v_exp_f32_e32 v75, v75
	v_rcp_f32_e32 v72, v72
	v_rcp_f32_e32 v73, v73
	v_add_f32_e32 v74, 1.0, v74
	v_add_f32_e32 v75, 1.0, v75
	v_rcp_f32_e32 v74, v74
	v_rcp_f32_e32 v75, v75
	v_mul_f32_e32 v72, v64, v72
	v_mul_f32_e32 v73, v65, v73
	v_mul_f32_e32 v74, v66, v74
	v_mul_f32_e32 v67, v67, v75
	v_cvt_pk_bf16_f32 v64, v68, v69
	v_cvt_pk_bf16_f32 v65, v70, v71
	v_cvt_pk_bf16_f32 v66, v72, v73
	v_add_u32_e32 v72, 0x90, v130
	v_cvt_pk_bf16_f32 v67, v74, v67
	global_store_dwordx4 v[90:91], v[64:67], off offset:256
	v_lshlrev_b32_e32 v78, 16, v209
	v_lshlrev_b32_e32 v76, 16, v208
	v_mad_i64_i32 v[64:65], s[6:7], v72, s51, v[132:133]
	v_lshl_add_u64 v[64:65], v[64:65], 0, v[128:129]
	s_nop 0
	v_mul_f32_e32 v77, 0xbfb8aa3b, v77
	v_mul_f32_e32 v78, 0xbfb8aa3b, v78
	v_mul_f32_e32 v76, 0xbfb8aa3b, v76
	v_exp_f32_e32 v77, v77
	v_exp_f32_e32 v78, v78
	v_exp_f32_e32 v76, v76
	v_and_b32_e32 v79, 0xffff0000, v209
	v_add_f32_e32 v77, 1.0, v77
	v_add_f32_e32 v78, 1.0, v78
	v_add_f32_e32 v76, 1.0, v76
	v_rcp_f32_e32 v77, v77
	v_rcp_f32_e32 v78, v78
	v_mul_f32_e32 v79, 0xbfb8aa3b, v79
	v_rcp_f32_e32 v76, v76
	v_exp_f32_e32 v79, v79
	v_mul_f32_e32 v61, v61, v77
	v_mul_f32_e32 v62, v62, v78
	v_lshlrev_b32_e32 v77, 16, v210
	v_and_b32_e32 v78, 0xffff0000, v210
	v_mul_f32_e32 v60, v60, v76
	v_add_f32_e32 v76, 1.0, v79
	v_mul_f32_e32 v77, 0xbfb8aa3b, v77
	v_mul_f32_e32 v78, 0xbfb8aa3b, v78
	v_rcp_f32_e32 v76, v76
	v_exp_f32_e32 v77, v77
	v_exp_f32_e32 v78, v78
	v_and_b32_e32 v79, 0xffff0000, v211
	v_mul_f32_e32 v63, v63, v76
	v_add_f32_e32 v76, 1.0, v77
	v_add_f32_e32 v77, 1.0, v78
	v_lshlrev_b32_e32 v78, 16, v211
	v_mul_f32_e32 v78, 0xbfb8aa3b, v78
	v_mul_f32_e32 v79, 0xbfb8aa3b, v79
	v_exp_f32_e32 v78, v78
	v_exp_f32_e32 v79, v79
	v_rcp_f32_e32 v76, v76
	v_rcp_f32_e32 v77, v77
	v_add_f32_e32 v78, 1.0, v78
	v_add_f32_e32 v79, 1.0, v79
	v_rcp_f32_e32 v78, v78
	v_rcp_f32_e32 v79, v79
	v_lshlrev_b64 v[74:75], 12, v[88:89]
	v_lshl_add_u64 v[74:75], s[2:3], 0, v[74:75]
	v_lshl_add_u64 v[74:75], v[74:75], 0, v[128:129]
	v_mul_f32_e32 v76, v56, v76
	v_mul_f32_e32 v77, v57, v77
	v_mul_f32_e32 v78, v58, v78
	v_mul_f32_e32 v59, v59, v79
	v_cvt_pk_bf16_f32 v56, v60, v61
	v_cvt_pk_bf16_f32 v57, v62, v63
	v_cvt_pk_bf16_f32 v58, v76, v77
	v_cvt_pk_bf16_f32 v59, v78, v59
	global_store_dwordx4 v[74:75], v[56:59], off
	v_ashrrev_i32_e32 v73, 31, v72
	s_waitcnt vmcnt(14)
	v_and_b32_e32 v61, 0xffff0000, v216
	v_and_b32_e32 v57, 0xffff0000, v212
	v_lshlrev_b32_e32 v58, 16, v213
	v_lshlrev_b32_e32 v56, 16, v212
	v_mul_f32_e32 v57, 0xbfb8aa3b, v57
	v_mul_f32_e32 v58, 0xbfb8aa3b, v58
	v_mul_f32_e32 v56, 0xbfb8aa3b, v56
	v_exp_f32_e32 v57, v57
	v_exp_f32_e32 v58, v58
	v_exp_f32_e32 v56, v56
	v_and_b32_e32 v59, 0xffff0000, v213
	v_add_f32_e32 v57, 1.0, v57
	v_add_f32_e32 v58, 1.0, v58
	v_add_f32_e32 v56, 1.0, v56
	v_rcp_f32_e32 v57, v57
	v_rcp_f32_e32 v58, v58
	v_mul_f32_e32 v59, 0xbfb8aa3b, v59
	v_rcp_f32_e32 v56, v56
	v_exp_f32_e32 v59, v59
	v_mul_f32_e32 v53, v53, v57
	v_mul_f32_e32 v54, v54, v58
	v_lshlrev_b32_e32 v57, 16, v214
	v_and_b32_e32 v58, 0xffff0000, v214
	v_mul_f32_e32 v52, v52, v56
	v_add_f32_e32 v56, 1.0, v59
	v_mul_f32_e32 v57, 0xbfb8aa3b, v57
	v_mul_f32_e32 v58, 0xbfb8aa3b, v58
	v_rcp_f32_e32 v56, v56
	v_exp_f32_e32 v57, v57
	v_exp_f32_e32 v58, v58
	v_and_b32_e32 v59, 0xffff0000, v215
	v_mul_f32_e32 v55, v55, v56
	v_add_f32_e32 v56, 1.0, v57
	v_add_f32_e32 v57, 1.0, v58
	v_lshlrev_b32_e32 v58, 16, v215
	v_mul_f32_e32 v58, 0xbfb8aa3b, v58
	v_mul_f32_e32 v59, 0xbfb8aa3b, v59
	v_exp_f32_e32 v58, v58
	v_exp_f32_e32 v59, v59
	v_rcp_f32_e32 v56, v56
	v_rcp_f32_e32 v57, v57
	v_add_f32_e32 v58, 1.0, v58
	v_add_f32_e32 v59, 1.0, v59
	v_rcp_f32_e32 v58, v58
	v_rcp_f32_e32 v59, v59
	v_mul_f32_e32 v56, v48, v56
	v_mul_f32_e32 v57, v49, v57
	v_mul_f32_e32 v58, v50, v58
	v_mul_f32_e32 v51, v51, v59
	v_cvt_pk_bf16_f32 v48, v52, v53
	v_cvt_pk_bf16_f32 v49, v54, v55
	v_cvt_pk_bf16_f32 v50, v56, v57
	v_add_u32_e32 v56, 0xa0, v130
	v_cvt_pk_bf16_f32 v51, v58, v51
	global_store_dwordx4 v[74:75], v[48:51], off offset:256
	v_lshlrev_b32_e32 v62, 16, v217
	v_lshlrev_b32_e32 v60, 16, v216
	v_mad_i64_i32 v[48:49], s[6:7], v56, s51, v[132:133]
	v_lshl_add_u64 v[48:49], v[48:49], 0, v[128:129]
	v_mul_f32_e32 v61, 0xbfb8aa3b, v61
	v_mul_f32_e32 v62, 0xbfb8aa3b, v62
	s_nop 0
	v_mul_f32_e32 v60, 0xbfb8aa3b, v60
	v_exp_f32_e32 v61, v61
	v_exp_f32_e32 v62, v62
	v_exp_f32_e32 v60, v60
	v_and_b32_e32 v63, 0xffff0000, v217
	v_add_f32_e32 v61, 1.0, v61
	v_add_f32_e32 v62, 1.0, v62
	v_add_f32_e32 v60, 1.0, v60
	v_rcp_f32_e32 v61, v61
	v_rcp_f32_e32 v62, v62
	v_mul_f32_e32 v63, 0xbfb8aa3b, v63
	v_rcp_f32_e32 v60, v60
	v_exp_f32_e32 v63, v63
	v_mul_f32_e32 v45, v45, v61
	v_mul_f32_e32 v46, v46, v62
	v_lshlrev_b32_e32 v61, 16, v218
	v_and_b32_e32 v62, 0xffff0000, v218
	v_mul_f32_e32 v44, v44, v60
	v_add_f32_e32 v60, 1.0, v63
	v_mul_f32_e32 v61, 0xbfb8aa3b, v61
	v_mul_f32_e32 v62, 0xbfb8aa3b, v62
	v_rcp_f32_e32 v60, v60
	v_exp_f32_e32 v61, v61
	v_exp_f32_e32 v62, v62
	v_and_b32_e32 v63, 0xffff0000, v219
	v_mul_f32_e32 v47, v47, v60
	v_add_f32_e32 v60, 1.0, v61
	v_add_f32_e32 v61, 1.0, v62
	v_lshlrev_b32_e32 v62, 16, v219
	v_mul_f32_e32 v62, 0xbfb8aa3b, v62
	v_mul_f32_e32 v63, 0xbfb8aa3b, v63
	v_exp_f32_e32 v62, v62
	v_exp_f32_e32 v63, v63
	v_rcp_f32_e32 v60, v60
	v_rcp_f32_e32 v61, v61
	v_add_f32_e32 v62, 1.0, v62
	v_add_f32_e32 v63, 1.0, v63
	v_rcp_f32_e32 v62, v62
	v_rcp_f32_e32 v63, v63
	v_lshlrev_b64 v[58:59], 12, v[72:73]
	v_lshl_add_u64 v[58:59], s[2:3], 0, v[58:59]
	v_lshl_add_u64 v[58:59], v[58:59], 0, v[128:129]
	v_mul_f32_e32 v60, v40, v60
	v_mul_f32_e32 v61, v41, v61
	v_mul_f32_e32 v62, v42, v62
	v_mul_f32_e32 v43, v43, v63
	v_cvt_pk_bf16_f32 v40, v44, v45
	v_cvt_pk_bf16_f32 v41, v46, v47
	v_cvt_pk_bf16_f32 v42, v60, v61
	v_cvt_pk_bf16_f32 v43, v62, v43
	global_store_dwordx4 v[58:59], v[40:43], off
	v_ashrrev_i32_e32 v57, 31, v56
	s_waitcnt vmcnt(14)
	v_and_b32_e32 v45, 0xffff0000, v224
	v_and_b32_e32 v41, 0xffff0000, v220
	v_lshlrev_b32_e32 v42, 16, v221
	v_lshlrev_b32_e32 v40, 16, v220
	v_mul_f32_e32 v41, 0xbfb8aa3b, v41
	v_mul_f32_e32 v42, 0xbfb8aa3b, v42
	v_mul_f32_e32 v40, 0xbfb8aa3b, v40
	v_exp_f32_e32 v41, v41
	v_exp_f32_e32 v42, v42
	v_exp_f32_e32 v40, v40
	v_and_b32_e32 v43, 0xffff0000, v221
	v_add_f32_e32 v41, 1.0, v41
	v_add_f32_e32 v42, 1.0, v42
	v_add_f32_e32 v40, 1.0, v40
	v_rcp_f32_e32 v41, v41
	v_rcp_f32_e32 v42, v42
	v_mul_f32_e32 v43, 0xbfb8aa3b, v43
	v_rcp_f32_e32 v40, v40
	v_exp_f32_e32 v43, v43
	v_mul_f32_e32 v37, v37, v41
	v_mul_f32_e32 v38, v38, v42
	v_lshlrev_b32_e32 v41, 16, v222
	v_and_b32_e32 v42, 0xffff0000, v222
	v_mul_f32_e32 v36, v36, v40
	v_add_f32_e32 v40, 1.0, v43
	v_mul_f32_e32 v41, 0xbfb8aa3b, v41
	v_mul_f32_e32 v42, 0xbfb8aa3b, v42
	v_rcp_f32_e32 v40, v40
	v_exp_f32_e32 v41, v41
	v_exp_f32_e32 v42, v42
	v_and_b32_e32 v43, 0xffff0000, v223
	v_mul_f32_e32 v39, v39, v40
	v_add_f32_e32 v40, 1.0, v41
	v_add_f32_e32 v41, 1.0, v42
	v_lshlrev_b32_e32 v42, 16, v223
	v_mul_f32_e32 v42, 0xbfb8aa3b, v42
	v_mul_f32_e32 v43, 0xbfb8aa3b, v43
	v_exp_f32_e32 v42, v42
	v_exp_f32_e32 v43, v43
	v_rcp_f32_e32 v40, v40
	v_rcp_f32_e32 v41, v41
	v_add_f32_e32 v42, 1.0, v42
	v_add_f32_e32 v43, 1.0, v43
	v_rcp_f32_e32 v42, v42
	v_rcp_f32_e32 v43, v43
	v_mul_f32_e32 v40, v32, v40
	v_mul_f32_e32 v41, v33, v41
	v_mul_f32_e32 v42, v34, v42
	v_mul_f32_e32 v35, v35, v43
	v_cvt_pk_bf16_f32 v32, v36, v37
	v_cvt_pk_bf16_f32 v33, v38, v39
	v_cvt_pk_bf16_f32 v34, v40, v41
	v_add_u32_e32 v40, 0xb0, v130
	v_cvt_pk_bf16_f32 v35, v42, v35
	global_store_dwordx4 v[58:59], v[32:35], off offset:256
	v_lshlrev_b32_e32 v46, 16, v225
	v_lshlrev_b32_e32 v44, 16, v224
	v_mad_i64_i32 v[32:33], s[6:7], v40, s51, v[132:133]
	v_lshl_add_u64 v[32:33], v[32:33], 0, v[128:129]
	s_nop 0
	v_mul_f32_e32 v45, 0xbfb8aa3b, v45
	v_mul_f32_e32 v46, 0xbfb8aa3b, v46
	v_mul_f32_e32 v44, 0xbfb8aa3b, v44
	v_exp_f32_e32 v45, v45
	v_exp_f32_e32 v46, v46
	v_exp_f32_e32 v44, v44
	v_and_b32_e32 v47, 0xffff0000, v225
	v_add_f32_e32 v45, 1.0, v45
	v_add_f32_e32 v46, 1.0, v46
	v_add_f32_e32 v44, 1.0, v44
	v_rcp_f32_e32 v45, v45
	v_rcp_f32_e32 v46, v46
	v_mul_f32_e32 v47, 0xbfb8aa3b, v47
	v_rcp_f32_e32 v44, v44
	v_exp_f32_e32 v47, v47
	v_mul_f32_e32 v29, v29, v45
	v_mul_f32_e32 v30, v30, v46
	v_lshlrev_b32_e32 v45, 16, v226
	v_and_b32_e32 v46, 0xffff0000, v226
	v_mul_f32_e32 v28, v28, v44
	v_add_f32_e32 v44, 1.0, v47
	v_mul_f32_e32 v45, 0xbfb8aa3b, v45
	v_mul_f32_e32 v46, 0xbfb8aa3b, v46
	v_rcp_f32_e32 v44, v44
	v_exp_f32_e32 v45, v45
	v_exp_f32_e32 v46, v46
	v_and_b32_e32 v47, 0xffff0000, v227
	v_mul_f32_e32 v31, v31, v44
	v_add_f32_e32 v44, 1.0, v45
	v_add_f32_e32 v45, 1.0, v46
	v_lshlrev_b32_e32 v46, 16, v227
	v_mul_f32_e32 v46, 0xbfb8aa3b, v46
	v_mul_f32_e32 v47, 0xbfb8aa3b, v47
	v_exp_f32_e32 v46, v46
	v_exp_f32_e32 v47, v47
	v_rcp_f32_e32 v44, v44
	v_rcp_f32_e32 v45, v45
	v_add_f32_e32 v46, 1.0, v46
	v_add_f32_e32 v47, 1.0, v47
	v_rcp_f32_e32 v46, v46
	v_rcp_f32_e32 v47, v47
	v_lshlrev_b64 v[42:43], 12, v[56:57]
	v_lshl_add_u64 v[42:43], s[2:3], 0, v[42:43]
	v_lshl_add_u64 v[42:43], v[42:43], 0, v[128:129]
	v_mul_f32_e32 v44, v24, v44
	v_mul_f32_e32 v45, v25, v45
	v_mul_f32_e32 v46, v26, v46
	v_mul_f32_e32 v27, v27, v47
	v_cvt_pk_bf16_f32 v24, v28, v29
	v_cvt_pk_bf16_f32 v25, v30, v31
	v_cvt_pk_bf16_f32 v26, v44, v45
	v_cvt_pk_bf16_f32 v27, v46, v27
	global_store_dwordx4 v[42:43], v[24:27], off
	v_ashrrev_i32_e32 v41, 31, v40
	s_mov_b64 s[6:7], -1
	s_waitcnt vmcnt(15)
	v_and_b32_e32 v25, 0xffff0000, v228
	v_lshlrev_b32_e32 v26, 16, v229
	v_lshlrev_b32_e32 v24, 16, v228
	v_mul_f32_e32 v25, 0xbfb8aa3b, v25
	v_mul_f32_e32 v26, 0xbfb8aa3b, v26
	v_mul_f32_e32 v24, 0xbfb8aa3b, v24
	v_exp_f32_e32 v25, v25
	v_exp_f32_e32 v26, v26
	v_exp_f32_e32 v24, v24
	v_and_b32_e32 v27, 0xffff0000, v229
	v_add_f32_e32 v25, 1.0, v25
	v_add_f32_e32 v26, 1.0, v26
	v_add_f32_e32 v24, 1.0, v24
	v_rcp_f32_e32 v25, v25
	v_rcp_f32_e32 v26, v26
	v_mul_f32_e32 v27, 0xbfb8aa3b, v27
	v_rcp_f32_e32 v24, v24
	v_exp_f32_e32 v27, v27
	v_mul_f32_e32 v21, v21, v25
	v_mul_f32_e32 v22, v22, v26
	v_lshlrev_b32_e32 v25, 16, v230
	v_and_b32_e32 v26, 0xffff0000, v230
	v_mul_f32_e32 v20, v20, v24
	v_add_f32_e32 v24, 1.0, v27
	v_mul_f32_e32 v25, 0xbfb8aa3b, v25
	v_mul_f32_e32 v26, 0xbfb8aa3b, v26
	v_rcp_f32_e32 v24, v24
	v_exp_f32_e32 v25, v25
	v_exp_f32_e32 v26, v26
	v_and_b32_e32 v27, 0xffff0000, v231
	v_mul_f32_e32 v23, v23, v24
	v_add_f32_e32 v24, 1.0, v25
	v_add_f32_e32 v25, 1.0, v26
	v_lshlrev_b32_e32 v26, 16, v231
	v_mul_f32_e32 v27, 0xbfb8aa3b, v27
	v_mul_f32_e32 v26, 0xbfb8aa3b, v26
	v_exp_f32_e32 v27, v27
	v_exp_f32_e32 v26, v26
	v_rcp_f32_e32 v24, v24
	v_rcp_f32_e32 v25, v25
	v_add_f32_e32 v27, 1.0, v27
	v_add_f32_e32 v26, 1.0, v26
	v_rcp_f32_e32 v27, v27
	v_rcp_f32_e32 v26, v26
	v_mul_f32_e32 v24, v16, v24
	v_mul_f32_e32 v25, v17, v25
	v_mul_f32_e32 v19, v19, v27
	v_mul_f32_e32 v26, v18, v26
	v_cvt_pk_bf16_f32 v16, v20, v21
	v_cvt_pk_bf16_f32 v17, v22, v23
	v_cvt_pk_bf16_f32 v18, v24, v25
	v_cvt_pk_bf16_f32 v19, v26, v19
	global_store_dwordx4 v[42:43], v[16:19], off offset:256
	s_waitcnt vmcnt(15)
	v_lshlrev_b32_e32 v20, 16, v233
	v_mul_f32_e32 v20, 0xbfb8aa3b, v20
	v_and_b32_e32 v19, 0xffff0000, v232
	v_lshlrev_b32_e32 v18, 16, v232
	v_mul_f32_e32 v19, 0xbfb8aa3b, v19
	v_mul_f32_e32 v18, 0xbfb8aa3b, v18
	v_exp_f32_e32 v19, v19
	v_exp_f32_e32 v20, v20
	v_exp_f32_e32 v18, v18
	v_and_b32_e32 v21, 0xffff0000, v233
	v_add_f32_e32 v19, 1.0, v19
	v_add_f32_e32 v20, 1.0, v20
	v_add_f32_e32 v18, 1.0, v18
	v_rcp_f32_e32 v19, v19
	v_rcp_f32_e32 v20, v20
	v_mul_f32_e32 v21, 0xbfb8aa3b, v21
	v_rcp_f32_e32 v18, v18
	v_exp_f32_e32 v21, v21
	v_mul_f32_e32 v13, v13, v19
	v_mul_f32_e32 v14, v14, v20
	v_lshlrev_b32_e32 v19, 16, v234
	v_and_b32_e32 v20, 0xffff0000, v234
	v_mul_f32_e32 v12, v12, v18
	v_add_f32_e32 v18, 1.0, v21
	v_mul_f32_e32 v19, 0xbfb8aa3b, v19
	v_mul_f32_e32 v20, 0xbfb8aa3b, v20
	v_rcp_f32_e32 v18, v18
	v_exp_f32_e32 v19, v19
	v_exp_f32_e32 v20, v20
	v_and_b32_e32 v21, 0xffff0000, v235
	v_mul_f32_e32 v15, v15, v18
	v_add_f32_e32 v18, 1.0, v19
	v_add_f32_e32 v19, 1.0, v20
	v_lshlrev_b32_e32 v20, 16, v235
	v_mul_f32_e32 v20, 0xbfb8aa3b, v20
	v_mul_f32_e32 v21, 0xbfb8aa3b, v21
	v_exp_f32_e32 v20, v20
	v_exp_f32_e32 v21, v21
	v_rcp_f32_e32 v18, v18
	v_rcp_f32_e32 v19, v19
	v_add_f32_e32 v20, 1.0, v20
	v_add_f32_e32 v21, 1.0, v21
	v_rcp_f32_e32 v20, v20
	v_rcp_f32_e32 v21, v21
	v_lshlrev_b64 v[16:17], 12, v[40:41]
	v_lshl_add_u64 v[16:17], s[2:3], 0, v[16:17]
	v_lshl_add_u64 v[16:17], v[16:17], 0, v[128:129]
	v_mul_f32_e32 v18, v8, v18
	v_mul_f32_e32 v19, v9, v19
	v_mul_f32_e32 v20, v10, v20
	v_mul_f32_e32 v11, v11, v21
	v_cvt_pk_bf16_f32 v8, v12, v13
	v_cvt_pk_bf16_f32 v9, v14, v15
	v_cvt_pk_bf16_f32 v10, v18, v19
	v_cvt_pk_bf16_f32 v11, v20, v11
	global_store_dwordx4 v[16:17], v[8:11], off
	s_nop 0
	s_waitcnt vmcnt(15)
	v_and_b32_e32 v9, 0xffff0000, v236
	v_lshlrev_b32_e32 v10, 16, v237
	v_lshlrev_b32_e32 v8, 16, v236
	v_mul_f32_e32 v9, 0xbfb8aa3b, v9
	v_mul_f32_e32 v10, 0xbfb8aa3b, v10
	v_mul_f32_e32 v8, 0xbfb8aa3b, v8
	v_exp_f32_e32 v9, v9
	v_exp_f32_e32 v10, v10
	v_exp_f32_e32 v8, v8
	v_and_b32_e32 v11, 0xffff0000, v237
	v_add_f32_e32 v9, 1.0, v9
	v_add_f32_e32 v10, 1.0, v10
	v_add_f32_e32 v8, 1.0, v8
	v_rcp_f32_e32 v9, v9
	v_rcp_f32_e32 v10, v10
	v_mul_f32_e32 v11, 0xbfb8aa3b, v11
	v_rcp_f32_e32 v8, v8
	v_exp_f32_e32 v11, v11
	v_mul_f32_e32 v5, v5, v9
	v_mul_f32_e32 v6, v6, v10
	v_lshlrev_b32_e32 v9, 16, v238
	v_and_b32_e32 v10, 0xffff0000, v238
	v_mul_f32_e32 v4, v4, v8
	v_add_f32_e32 v8, 1.0, v11
	v_mul_f32_e32 v9, 0xbfb8aa3b, v9
	v_mul_f32_e32 v10, 0xbfb8aa3b, v10
	v_rcp_f32_e32 v8, v8
	v_exp_f32_e32 v9, v9
	v_exp_f32_e32 v10, v10
	v_and_b32_e32 v11, 0xffff0000, v239
	v_mul_f32_e32 v7, v7, v8
	v_add_f32_e32 v8, 1.0, v9
	v_add_f32_e32 v9, 1.0, v10
	v_lshlrev_b32_e32 v10, 16, v239
	v_mul_f32_e32 v11, 0xbfb8aa3b, v11
	v_mul_f32_e32 v10, 0xbfb8aa3b, v10
	v_exp_f32_e32 v11, v11
	v_exp_f32_e32 v10, v10
	v_rcp_f32_e32 v8, v8
	v_rcp_f32_e32 v9, v9
	v_add_f32_e32 v11, 1.0, v11
	v_add_f32_e32 v10, 1.0, v10
	v_rcp_f32_e32 v11, v11
	v_rcp_f32_e32 v10, v10
	v_mul_f32_e32 v8, v0, v8
	v_mul_f32_e32 v9, v1, v9
	v_mul_f32_e32 v3, v3, v11
	v_mul_f32_e32 v10, v2, v10
	v_cvt_pk_bf16_f32 v0, v4, v5
	v_cvt_pk_bf16_f32 v1, v6, v7
	v_cvt_pk_bf16_f32 v2, v8, v9
	v_cvt_pk_bf16_f32 v3, v10, v3
	global_store_dwordx4 v[16:17], v[0:3], off offset:256
	s_cbranch_vccnz .LBB0_2171
	s_andn2_b64 vcc, exec, s[0:1]
	s_cbranch_vccnz .LBB0_2170
	s_barrier
	s_branch .LBB0_2170
